# drop the unit-start rendezvous in the expert GEMMs: lagging half skips its re-offset and prologue stagger barriers, leading half skips the pre-MMA barrier of each unit's first K step
# baseline (speedup 1.0000x reference)
; #define PG8_STAGEB(bufoff, gbase) glds2(voffB, (gbase), voffB, (gbase) + qstep, ldsb + (bufoff))
; template <class Epi, bool GATHER, int MODE, bool SPLIT = false>
; __device__ __forceinline__ void gemm_phase(PG8_LAS unsigned char* lds, const Gemm g, const Order& S, const Epi& E) {
;     ...
;     const int tid = tid_, wid = __builtin_amdgcn_readfirstlane(tid >> 6), lane = tid & 63, wr = wid >> 2, wc = wid & 3, fr = lane & 15, fq = lane >> 4;
;     const int RB = g.rowbytes, nt = RB / 128;
;     int R0, C0; stage_rc(tid * 16, R0, C0);
;     const int Rb0 = Epi::PERM ? ((R0 & ~31) + perm32(R0 & 31)) : R0;
;     const unsigned voffB = (unsigned)(Rb0 * RB + C0 * 2), voffA = (unsigned)(R0 * RB + C0 * 2);
;     const size_t kstep = (size_t)(BK * 2);
;     const size_t qstep = (size_t)64 * RB;
;     const size_t hstep = (size_t)HALF * RB;
;     const size_t tstep = 2 * hstep;
;     const unsigned ldsb = (unsigned)(size_t)lds + (unsigned)wid * 1024u;
;     const int aoff = lds_byte(wr * 64 + fr, fq * 8), boff = lds_byte(wc * 32 + fr, fq * 8);
;     ...
;     Unit cur, nxt; int ui = 0;
;     if (!S.next(0, cur)) return;
;     f32x4 acc[2][2][4][2];
; #pragma unroll
;     for (int a = 0; a < 2; ++a)
; #pragma unroll
;         for (int b = 0; b < 2; ++b)
; #pragma unroll
;             for (int m = 0; m < 4; ++m)
; #pragma unroll
;                 for (int n = 0; n < 2; ++n) acc[a][b][m][n] = (f32x4){0.f, 0.f, 0.f, 0.f};
;     bf16x8 At[4][2], B0[2][2], B1[2][2];
;     unsigned cv[2][2] = {{0u, 0u}, {0u, 0u}}, nv[2][2] = {{0u, 0u}, {0u, 0u}};
;     PG8_VOFF(cv, cur);
;     const char* const Ab = (const char*)g.A;
;     size_t cAr = (size_t)cur.pm * tstep;
;     const char* cB = (const char*)g.Bt + (size_t)cur.e * g.bstride + (size_t)cur.pn * tstep;
;     PG8_STAGEB(PG8_SB(0, 0), cB); PG8_STAGEB(PG8_SB(0, 1), cB + hstep); PG8_STAGEA(PG8_SA(0, 0), cAr, cv, 0, 0); PG8_STAGEA(PG8_SA(0, 1), cAr, cv, 1, 0);
;     if (wr == 1) PG8_BAR;
; __global__ void __launch_bounds__(NWAVES * 64, 2) fwd_kernel(Args args) {
;     ...
;     if (IN(8)) {
;         const int* TILEE = (const int*)(ws + WS_TILEE);
;         const int ntiles = __builtin_amdgcn_readfirstlane(TILEE[512]);
;         pg8::Gemm g{ws + WS_H8, ws + WS_WGU, D, (size_t)2 * DFF * D, (const int*)(ws + WS_SLOTTOK), (const float*)(ws + WS_RSSLOT)};
;         pg8::Order S; S.init(ntiles, 2 * DFF / 256, F.G, (int)blockIdx.x, TILEE, WGM_GU);
.LBB0_790:
	s_cmp_lt_i32 s78, 9
	s_cselect_b64 s[0:1], -1, 0
	s_cmp_gt_i32 s79, 8
	s_cselect_b64 s[2:3], -1, 0
	s_and_b64 s[0:1], s[0:1], s[2:3]
	s_andn2_b64 vcc, exec, s[0:1]
	s_cbranch_vccnz .LBB0_863
	v_mov_b32_e32 v1, 0xc00000
	global_load_dword v1, v1, s[76:77] offset:2048
	s_waitcnt vmcnt(20)
	v_mov_b32_e32 v2, v0
	s_waitcnt vmcnt(0)
	v_readfirstlane_b32 s38, v1
	s_lshl_b32 s2, s38, 4
	s_cmp_ge_i32 s92, s2
	v_readfirstlane_b32 s3, v2
	s_cbranch_scc1 .LBB0_809
	s_add_u32 s39, s76, 0xc00000
	s_addc_u32 s40, s77, 0
	s_add_u32 s6, s76, 0x5b000000
	s_addc_u32 s7, s77, 0
	s_add_u32 s41, s76, 0x28000000
	s_addc_u32 s42, s77, 0
	s_add_u32 s8, s76, 0xb00000
	s_addc_u32 s9, s77, 0
	s_ashr_i32 s4, s3, 6
	s_lshl_b32 s0, s4, 10
	s_ashr_i32 s45, s92, 31
	s_add_i32 s43, s0, 0
	s_lshr_b32 s0, s45, 29
	s_add_i32 s0, s92, s0
	s_lshl_b32 s44, s38, 1
	s_ashr_i32 s1, s0, 3
	s_and_b32 s0, s0, -8
	s_ashr_i32 s5, s3, 8
	s_sub_i32 s0, s92, s0
	s_or_b32 s46, s44, 1
	s_cmp_lt_i32 s0, 0
	s_cselect_b32 s10, s46, s44
	s_mul_i32 s0, s10, s0
	s_add_i32 s0, s0, s1
	s_ashr_i32 s1, s0, 31
	s_lshr_b32 s1, s1, 26
	s_add_i32 s1, s0, s1
	v_bfe_i32 v4, v2, 27, 1
	s_ashr_i32 s10, s1, 6
	v_lshlrev_b32_e32 v1, 4, v2
	v_lshrrev_b32_e32 v4, 22, v4
	s_lshl_b32 s10, s10, 2
	v_add_u32_e32 v4, v1, v4
	s_sub_i32 s11, s38, s10
	v_and_b32_e32 v4, 0xfffffc00, v4
	s_min_i32 s11, s11, 4
	v_sub_u32_e32 v1, v1, v4
	s_abs_i32 s12, s11
	v_lshrrev_b32_e32 v4, 4, v1
	v_cvt_f32_u32_e32 v5, s12
	v_bitop3_b32 v12, v4, v1, 32 bitop3:0x6c
	v_ashrrev_i32_e32 v4, 31, v12
	v_lshrrev_b32_e32 v4, 26, v4
	v_add_u32_e32 v13, v12, v4
	v_rcp_iflag_f32_e32 v4, v5
	s_sub_i32 s14, 0, s12
	s_andn2_b32 s1, s1, 63
	s_sub_i32 s1, s0, s1
	v_mul_f32_e32 v4, 0x4f7ffffe, v4
	v_cvt_u32_f32_e32 v4, v4
	s_abs_i32 s13, s1
	s_xor_b32 s0, s1, s11
	s_ashr_i32 s0, s0, 31
	v_readfirstlane_b32 s15, v4
	s_mul_i32 s14, s14, s15
	s_mul_hi_u32 s14, s15, s14
	s_add_i32 s15, s15, s14
	s_mul_hi_u32 s14, s13, s15
	s_mul_i32 s15, s14, s12
	s_sub_i32 s13, s13, s15
	s_add_i32 s15, s14, 1
	s_sub_i32 s16, s13, s12
	s_cmp_ge_u32 s13, s12
	s_cselect_b32 s14, s15, s14
	s_cselect_b32 s13, s16, s13
	s_add_i32 s15, s14, 1
	v_ashrrev_i32_e32 v3, 31, v2
	s_cmp_ge_u32 s13, s12
	v_lshrrev_b32_e32 v3, 26, v3
	s_cselect_b32 s12, s15, s14
	v_add_u32_e32 v3, v2, v3
	s_xor_b32 s12, s12, s0
	v_ashrrev_i32_e32 v3, 6, v3
	s_sub_i32 s0, s12, s0
	v_lshlrev_b32_e32 v1, 3, v3
	s_mul_i32 s11, s0, s11
	v_and_b32_e32 v1, -16, v1
	v_ashrrev_i32_e32 v14, 6, v13
	s_sub_i32 s1, s1, s11
	v_add_u32_e32 v1, v14, v1
	s_add_i32 s10, s10, s1
	s_ashr_i32 s11, s10, 31
	v_lshl_add_u32 v4, s10, 8, v1
	s_lshl_b64 s[12:13], s[10:11], 2
	v_ashrrev_i32_e32 v5, 31, v4
	s_add_u32 s12, s39, s12
	v_lshl_add_u64 v[6:7], v[4:5], 2, s[8:9]
	v_add_u32_e32 v8, 64, v4
	v_add_u32_e32 v10, 0x80, v4
	v_add_u32_e32 v4, 0xc0, v4
	s_addc_u32 s13, s40, s13
	v_mov_b32_e32 v166, 0
	v_ashrrev_i32_e32 v9, 31, v8
	v_ashrrev_i32_e32 v11, 31, v10
	v_ashrrev_i32_e32 v5, 31, v4
	v_lshl_add_u64 v[8:9], v[8:9], 2, s[8:9]
	v_lshl_add_u64 v[10:11], v[10:11], 2, s[8:9]
	v_lshl_add_u64 v[4:5], v[4:5], 2, s[8:9]
	global_load_dword v164, v166, s[12:13]
	global_load_dword v15, v[6:7], off
	global_load_dword v16, v[8:9], off
	global_load_dword v17, v[10:11], off
	global_load_dword v18, v[4:5], off
	s_mov_b32 s1, 0x1fffe0
	v_and_b32_e32 v6, 3, v14
	v_and_or_b32 v6, v1, s1, v6
	v_and_b32_e32 v5, 0xc0, v13
	v_mov_b32_e32 v4, 1
	v_sub_u32_e32 v5, v12, v5
	v_lshlrev_b32_e32 v3, 5, v3
	v_ashrrev_i16_sdwa v4, v4, sext(v5) dst_sel:DWORD dst_unused:UNUSED_PAD src0_sel:DWORD src1_sel:BYTE_0
	v_lshlrev_b32_e32 v5, 1, v1
	v_lshrrev_b32_e32 v7, 2, v1
	v_and_b32_e32 v3, 32, v3
	v_bfe_i32 v4, v4, 0, 16
	v_and_b32_e32 v5, 24, v5
	v_and_b32_e32 v7, 4, v7
	v_or3_b32 v5, v6, v7, v5
	v_add_lshl_u32 v167, v3, v4, 1
	v_lshl_add_u32 v168, v5, 11, v167
	s_mov_b32 s47, 0
	s_movk_i32 s48, 0x2000
	s_waitcnt vmcnt(4)
	v_readfirstlane_b32 s12, v164
	s_ashr_i32 s13, s12, 31
	s_lshl_b64 s[12:13], s[12:13], 23
	s_add_u32 s11, s41, s12
	s_addc_u32 s14, s42, s13
	s_ashr_i32 s1, s0, 31
	s_lshl_b64 s[12:13], s[0:1], 19
	s_add_u32 s34, s11, s12
	s_addc_u32 s35, s14, s13
	s_add_u32 s12, s34, 0x20000
	s_addc_u32 s13, s35, 0
	s_add_i32 s49, s43, 0x10000
	s_add_i32 s50, s43, 0x12000
	s_mov_b32 s1, m0
	s_mov_b32 m0, s49
	s_nop 0
	global_load_lds_dwordx4 v168, s[34:35]
	s_mov_b32 m0, s50
	s_nop 0
	global_load_lds_dwordx4 v168, s[12:13]
	s_mov_b32 m0, s1
	s_add_u32 s12, s34, 0x40000
	s_addc_u32 s13, s35, 0
	s_add_u32 s14, s34, 0x60000
	s_addc_u32 s15, s35, 0
	s_add_i32 s51, s43, 0x14000
	s_add_i32 s52, s43, 0x16000
	s_mov_b32 s1, m0
	s_mov_b32 m0, s51
	s_nop 0
	global_load_lds_dwordx4 v168, s[12:13]
	s_mov_b32 m0, s52
	s_nop 0
	global_load_lds_dwordx4 v168, s[14:15]
	s_mov_b32 m0, s1
	s_waitcnt vmcnt(3)
	v_lshl_add_u32 v191, v15, 11, v167
	s_waitcnt vmcnt(2)
	v_lshl_add_u32 v192, v16, 11, v167
	s_add_i32 s53, s43, 0x2000
	s_mov_b32 s1, m0
	s_mov_b32 m0, s43
	s_nop 0
	global_load_lds_dwordx4 v191, s[6:7]
	s_mov_b32 m0, s53
	s_nop 0
	global_load_lds_dwordx4 v192, s[6:7]
	s_mov_b32 m0, s1
	s_waitcnt vmcnt(1)
	v_lshl_add_u32 v189, v17, 11, v167
	s_waitcnt vmcnt(0)
	v_lshl_add_u32 v190, v18, 11, v167
	s_add_i32 s54, s43, 0x4000
	s_add_i32 s55, s43, 0x6000
	s_mov_b32 s1, m0
	s_mov_b32 m0, s54
	s_nop 0
	global_load_lds_dwordx4 v189, s[6:7]
	s_mov_b32 m0, s55
	s_nop 0
	global_load_lds_dwordx4 v190, s[6:7]
	s_mov_b32 m0, s1
	s_cmp_eq_u32 s5, 1
	s_cselect_b64 s[12:13], -1, 0
	s_cmp_lg_u32 s5, 1
	s_cbranch_scc1 .LBB0_794
	s_nop 0

; #define PG8_STAGEB(bufoff, gbase) glds2(voffB, (gbase), voffB, (gbase) + qstep, ldsb + (bufoff))
; #define PG8_STAGEA(bufoff, rowb, v, h, kb) do { if constexpr (GATHER) glds2((v)[h][0], Ab + (kb), (v)[h][1], Ab + (kb), ldsb + (bufoff)); \
;         else glds2(voffA, Ab + (rowb) + (h) * hstep + (kb), voffA, Ab + (rowb) + (h) * hstep + qstep + (kb), ldsb + (bufoff)); } while (0)
; #define PG8_LDA(dst, b, h) do { _Pragma("unroll") for (int m = 0; m < 4; ++m) _Pragma("unroll") for (int k = 0; k < 2; ++k) dst[m][k] = *(const PG8_LAS bf16x8*)(lds + PG8_SA(b, h) + aoff + m * 2048 + k * 1024); } while (0)
; #define PG8_LDB(dst, b, h) do { _Pragma("unroll") for (int n = 0; n < 2; ++n) _Pragma("unroll") for (int k = 0; k < 2; ++k) dst[n][k] = *(const PG8_LAS bf16x8*)(lds + PG8_SB(b, h) + boff + n * 2048 + k * 1024); } while (0)
; #define PG8_WAIT_V(n) asm volatile("s_waitcnt vmcnt(" #n ")" ::: "memory")
; #define PG8_WAIT_L(n) asm volatile("s_waitcnt lgkmcnt(" #n ")" ::: "memory")
; #define PG8_BAR __builtin_amdgcn_s_barrier()
; #define PG8_SCHED __builtin_amdgcn_sched_barrier(0)
; template <class Epi, bool GATHER, int MODE, bool SPLIT = false>
; __device__ __forceinline__ void gemm_phase(PG8_LAS unsigned char* lds, const Gemm g, const Order& S, const Epi& E) {
;     ...
;             const size_t k1 = (size_t)(t + 1) * kstep, k2 = k1 + kstep, k3 = k2 + kstep;
;             const char* b2 = cB + k2; const char* b3 = cB + k3;
;             PG8_LDB(B0, 0, 0); PG8_LDB(B1, 0, 1); PG8_SCHED; PG8_LDA(At, 0, 0); PG8_STAGEA(PG8_SA(1, 1), cAr, cv, 1, k1);
;             PG8_WAIT_V(8); PG8_WAIT_L(0); PG8_BAR; PG8_MMA(0, 0, At, B0); PG8_MMA(0, 1, At, B1); PG8_BAR; PG8_SCHED;
;             PG8_LDA(At, 0, 1); PG8_STAGEB(PG8_SB(0, 0), b2); PG8_STAGEB(PG8_SB(0, 1), b2 + hstep); PG8_STAGEA(PG8_SA(0, 0), cAr, cv, 0, k2);
;             PG8_WAIT_V(8); PG8_WAIT_L(0); PG8_BAR; PG8_MMA(1, 0, At, B0); PG8_MMA(1, 1, At, B1); PG8_BAR; PG8_SCHED;
.LBB0_802:
	ds_read_b128 v[158:161], v179
	ds_read_b128 v[150:153], v179 offset:1024
	ds_read_b128 v[154:157], v179 offset:2048
	ds_read_b128 v[146:149], v179 offset:3072
	ds_read_b128 v[142:145], v180
	ds_read_b128 v[130:133], v180 offset:1024
	ds_read_b128 v[138:141], v180 offset:2048
	ds_read_b128 v[134:137], v180 offset:3072
	s_add_u32 s66, s34, s30
	s_addc_u32 s67, s35, s31
	s_add_u32 s36, s66, 0x100
	s_addc_u32 s37, s67, 0
	ds_read_b128 v[194:197], v181
	ds_read_b128 v[198:201], v181 offset:1024
	ds_read_b128 v[202:205], v181 offset:2048
	ds_read_b128 v[206:209], v181 offset:3072
	ds_read_b128 v[210:213], v181 offset:4096
	ds_read_b128 v[214:217], v181 offset:5120
	ds_read_b128 v[218:221], v181 offset:6144
	ds_read_b128 v[222:225], v181 offset:7168
	s_add_u32 s27, s6, s30
	s_addc_u32 s29, s7, s31
	s_add_u32 s68, s27, 0x80
	s_addc_u32 s69, s29, 0
	s_mov_b32 s70, m0
	s_mov_b32 m0, s62
	s_nop 0
	global_load_lds_dwordx4 v189, s[68:69]
	s_mov_b32 m0, s63
	s_nop 0
	global_load_lds_dwordx4 v190, s[68:69]
	s_mov_b32 m0, s70
	s_waitcnt vmcnt(8)
	s_waitcnt lgkmcnt(0)
	s_cmp_eq_i32 s11, -2
	s_cselect_b64 vcc, s[22:23], 0
	s_cbranch_vccnz .Lfb8
	s_barrier
.Lfb8:
	s_setprio 1
	s_waitcnt lgkmcnt(7)
	v_mfma_i32_16x16x64_i8 v[126:129], v[158:161], v[194:197], v[126:129]
	v_mfma_i32_16x16x64_i8 v[122:125], v[154:157], v[194:197], v[122:125]
	s_waitcnt lgkmcnt(5)
	v_mfma_i32_16x16x64_i8 v[118:121], v[158:161], v[202:205], v[118:121]
	v_mfma_i32_16x16x64_i8 v[106:109], v[154:157], v[202:205], v[106:109]
	s_waitcnt lgkmcnt(3)
	v_mfma_i32_16x16x64_i8 v[102:105], v[158:161], v[210:213], v[102:105]
	v_mfma_i32_16x16x64_i8 v[90:93], v[154:157], v[210:213], v[90:93]
	s_waitcnt lgkmcnt(1)
	v_mfma_i32_16x16x64_i8 v[86:89], v[158:161], v[218:221], v[86:89]
	v_mfma_i32_16x16x64_i8 v[74:77], v[154:157], v[218:221], v[74:77]
	v_mfma_i32_16x16x64_i8 v[126:129], v[150:153], v[198:201], v[126:129]
	v_mfma_i32_16x16x64_i8 v[122:125], v[146:149], v[198:201], v[122:125]
	v_mfma_i32_16x16x64_i8 v[118:121], v[150:153], v[206:209], v[118:121]
	v_mfma_i32_16x16x64_i8 v[106:109], v[146:149], v[206:209], v[106:109]
	v_mfma_i32_16x16x64_i8 v[102:105], v[150:153], v[214:217], v[102:105]
	v_mfma_i32_16x16x64_i8 v[90:93], v[146:149], v[214:217], v[90:93]
	s_waitcnt lgkmcnt(0)
	v_mfma_i32_16x16x64_i8 v[86:89], v[150:153], v[222:225], v[86:89]
	v_mfma_i32_16x16x64_i8 v[74:77], v[146:149], v[222:225], v[74:77]
	s_setprio 0
	s_setprio 1
	v_mfma_i32_16x16x64_i8 v[114:117], v[142:145], v[194:197], v[114:117]
	v_mfma_i32_16x16x64_i8 v[110:113], v[138:141], v[194:197], v[110:113]
	v_mfma_i32_16x16x64_i8 v[98:101], v[142:145], v[202:205], v[98:101]
	v_mfma_i32_16x16x64_i8 v[94:97], v[138:141], v[202:205], v[94:97]
	v_mfma_i32_16x16x64_i8 v[82:85], v[142:145], v[210:213], v[82:85]
	v_mfma_i32_16x16x64_i8 v[78:81], v[138:141], v[210:213], v[78:81]
	v_mfma_i32_16x16x64_i8 v[70:73], v[142:145], v[218:221], v[70:73]
	v_mfma_i32_16x16x64_i8 v[66:69], v[138:141], v[218:221], v[66:69]
	s_nop 0
	v_mfma_i32_16x16x64_i8 v[114:117], v[130:133], v[198:201], v[114:117]
	v_mfma_i32_16x16x64_i8 v[110:113], v[134:137], v[198:201], v[110:113]
	v_mfma_i32_16x16x64_i8 v[98:101], v[130:133], v[206:209], v[98:101]
	v_mfma_i32_16x16x64_i8 v[94:97], v[134:137], v[206:209], v[94:97]
	v_mfma_i32_16x16x64_i8 v[82:85], v[130:133], v[214:217], v[82:85]
	v_mfma_i32_16x16x64_i8 v[78:81], v[134:137], v[214:217], v[78:81]
	v_mfma_i32_16x16x64_i8 v[70:73], v[130:133], v[222:225], v[70:73]
	v_mfma_i32_16x16x64_i8 v[66:69], v[134:137], v[222:225], v[66:69]
	s_setprio 0
	s_barrier
	s_add_u32 s68, s66, 0x20100
	s_addc_u32 s69, s67, 0
	ds_read_b128 v[194:197], v181 offset:16384
	ds_read_b128 v[198:201], v181 offset:17408
	ds_read_b128 v[202:205], v181 offset:18432
	ds_read_b128 v[206:209], v181 offset:19456
	ds_read_b128 v[210:213], v181 offset:20480
	ds_read_b128 v[214:217], v181 offset:21504
	ds_read_b128 v[218:221], v181 offset:22528
	ds_read_b128 v[222:225], v181 offset:23552
	s_mov_b32 s70, m0
	s_mov_b32 m0, s49
	s_nop 0
	global_load_lds_dwordx4 v168, s[36:37]
	s_mov_b32 m0, s50
	s_nop 0
	global_load_lds_dwordx4 v168, s[68:69]
	s_mov_b32 m0, s70
	s_add_u32 s36, s66, 0x40100
	s_addc_u32 s37, s67, 0
	s_add_u32 s68, s66, 0x60100
	s_addc_u32 s69, s67, 0
	s_mov_b32 s70, m0
	s_mov_b32 m0, s51
	s_nop 0
	global_load_lds_dwordx4 v168, s[36:37]
	s_mov_b32 m0, s52
	s_nop 0
	global_load_lds_dwordx4 v168, s[68:69]
	s_mov_b32 m0, s70
	s_add_u32 s36, s27, 0x100
	s_addc_u32 s37, s29, 0
	s_mov_b32 s68, m0
	s_mov_b32 m0, s43
	s_nop 0
	global_load_lds_dwordx4 v191, s[36:37]
	s_mov_b32 m0, s53
	s_nop 0
	global_load_lds_dwordx4 v192, s[36:37]
	s_mov_b32 m0, s68
	s_waitcnt vmcnt(8)
	s_waitcnt lgkmcnt(0)
	s_barrier
; #define PG8_STAGEB(bufoff, gbase) glds2(voffB, (gbase), voffB, (gbase) + qstep, ldsb + (bufoff))
; #define PG8_STAGEA(bufoff, rowb, v, h, kb) do { if constexpr (GATHER) glds2((v)[h][0], Ab + (kb), (v)[h][1], Ab + (kb), ldsb + (bufoff)); \
;         else glds2(voffA, Ab + (rowb) + (h) * hstep + (kb), voffA, Ab + (rowb) + (h) * hstep + qstep + (kb), ldsb + (bufoff)); } while (0)
; #define PG8_LDA(dst, b, h) do { _Pragma("unroll") for (int m = 0; m < 4; ++m) _Pragma("unroll") for (int k = 0; k < 2; ++k) dst[m][k] = *(const PG8_LAS bf16x8*)(lds + PG8_SA(b, h) + aoff + m * 2048 + k * 1024); } while (0)
; #define PG8_LDB(dst, b, h) do { _Pragma("unroll") for (int n = 0; n < 2; ++n) _Pragma("unroll") for (int k = 0; k < 2; ++k) dst[n][k] = *(const PG8_LAS bf16x8*)(lds + PG8_SB(b, h) + boff + n * 2048 + k * 1024); } while (0)
; #define PG8_WAIT_V(n) asm volatile("s_waitcnt vmcnt(" #n ")" ::: "memory")
; #define PG8_WAIT_L(n) asm volatile("s_waitcnt lgkmcnt(" #n ")" ::: "memory")
; #define PG8_BAR __builtin_amdgcn_s_barrier()
; #define PG8_SCHED __builtin_amdgcn_sched_barrier(0)
; template <class Epi, bool GATHER, int MODE, bool SPLIT = false>
; __device__ __forceinline__ void gemm_phase(PG8_LAS unsigned char* lds, const Gemm g, const Order& S, const Epi& E) {
;     ...
;             PG8_WAIT_V(8); PG8_WAIT_L(0); PG8_BAR; PG8_MMA(1, 0, At, B0); PG8_MMA(1, 1, At, B1); PG8_BAR; PG8_SCHED;
;             PG8_LDB(B0, 1, 0); PG8_LDB(B1, 1, 1); PG8_SCHED; PG8_LDA(At, 1, 0); PG8_STAGEA(PG8_SA(0, 1), cAr, cv, 1, k2);
;             PG8_WAIT_V(8); PG8_WAIT_L(0); PG8_BAR; PG8_MMA(0, 0, At, B0); PG8_MMA(0, 1, At, B1); PG8_BAR; PG8_SCHED;
;             PG8_LDA(At, 1, 1); PG8_STAGEB(PG8_SB(1, 0), b3); PG8_STAGEB(PG8_SB(1, 1), b3 + hstep); PG8_STAGEA(PG8_SA(1, 0), cAr, cv, 0, k3);
	s_setprio 1
	s_waitcnt lgkmcnt(7)
	v_mfma_i32_16x16x64_i8 v[62:65], v[158:161], v[194:197], v[62:65]
	v_mfma_i32_16x16x64_i8 v[58:61], v[154:157], v[194:197], v[58:61]
	s_waitcnt lgkmcnt(5)
	v_mfma_i32_16x16x64_i8 v[46:49], v[158:161], v[202:205], v[46:49]
	v_mfma_i32_16x16x64_i8 v[42:45], v[154:157], v[202:205], v[42:45]
	s_waitcnt lgkmcnt(3)
	v_mfma_i32_16x16x64_i8 v[38:41], v[158:161], v[210:213], v[38:41]
	v_mfma_i32_16x16x64_i8 v[34:37], v[154:157], v[210:213], v[34:37]
	s_waitcnt lgkmcnt(1)
	v_mfma_i32_16x16x64_i8 v[22:25], v[158:161], v[218:221], v[22:25]
	v_mfma_i32_16x16x64_i8 v[18:21], v[154:157], v[218:221], v[18:21]
	v_mfma_i32_16x16x64_i8 v[62:65], v[150:153], v[198:201], v[62:65]
	v_mfma_i32_16x16x64_i8 v[58:61], v[146:149], v[198:201], v[58:61]
	v_mfma_i32_16x16x64_i8 v[46:49], v[150:153], v[206:209], v[46:49]
	v_mfma_i32_16x16x64_i8 v[42:45], v[146:149], v[206:209], v[42:45]
	v_mfma_i32_16x16x64_i8 v[38:41], v[150:153], v[214:217], v[38:41]
	v_mfma_i32_16x16x64_i8 v[34:37], v[146:149], v[214:217], v[34:37]
	s_waitcnt lgkmcnt(0)
	v_mfma_i32_16x16x64_i8 v[22:25], v[150:153], v[222:225], v[22:25]
	v_mfma_i32_16x16x64_i8 v[18:21], v[146:149], v[222:225], v[18:21]
	s_setprio 0
	s_setprio 1
	v_mfma_i32_16x16x64_i8 v[54:57], v[142:145], v[194:197], v[54:57]
	v_mfma_i32_16x16x64_i8 v[50:53], v[138:141], v[194:197], v[50:53]
	v_mfma_i32_16x16x64_i8 v[30:33], v[142:145], v[202:205], v[30:33]
	v_mfma_i32_16x16x64_i8 v[26:29], v[138:141], v[202:205], v[26:29]
	v_mfma_i32_16x16x64_i8 v[14:17], v[142:145], v[210:213], v[14:17]
	v_mfma_i32_16x16x64_i8 v[10:13], v[138:141], v[210:213], v[10:13]
	v_mfma_i32_16x16x64_i8 v[6:9], v[142:145], v[218:221], v[6:9]
	v_mfma_i32_16x16x64_i8 v[2:5], v[138:141], v[218:221], v[2:5]
	s_nop 0
	v_mfma_i32_16x16x64_i8 v[54:57], v[130:133], v[198:201], v[54:57]
	v_mfma_i32_16x16x64_i8 v[50:53], v[134:137], v[198:201], v[50:53]
	v_mfma_i32_16x16x64_i8 v[30:33], v[130:133], v[206:209], v[30:33]
	v_mfma_i32_16x16x64_i8 v[26:29], v[134:137], v[206:209], v[26:29]
	v_mfma_i32_16x16x64_i8 v[14:17], v[130:133], v[214:217], v[14:17]
	v_mfma_i32_16x16x64_i8 v[10:13], v[134:137], v[214:217], v[10:13]
	v_mfma_i32_16x16x64_i8 v[6:9], v[130:133], v[222:225], v[6:9]
	v_mfma_i32_16x16x64_i8 v[2:5], v[134:137], v[222:225], v[2:5]
	s_setprio 0
	s_barrier
	v_add_u32_e32 v138, 0x1c000, v178
	ds_read_b128 v[130:133], v182
	ds_read_b128 v[134:137], v182 offset:1024
	ds_read_b128 v[140:143], v182 offset:2048
	ds_read_b128 v[144:147], v182 offset:3072
	ds_read_b128 v[148:151], v138
	ds_read_b128 v[152:155], v138 offset:1024
	ds_read_b128 v[156:159], v138 offset:2048
	ds_read_b128 v[194:197], v138 offset:3072
	ds_read_b128 v[198:201], v181 offset:32768
	ds_read_b128 v[202:205], v181 offset:33792
	ds_read_b128 v[206:209], v181 offset:34816
	ds_read_b128 v[210:213], v181 offset:35840
	ds_read_b128 v[214:217], v181 offset:36864
	ds_read_b128 v[218:221], v181 offset:37888
	ds_read_b128 v[222:225], v181 offset:38912
	ds_read_b128 v[226:229], v181 offset:39936
	s_mov_b32 s68, m0
	s_mov_b32 m0, s54
	s_nop 0
	global_load_lds_dwordx4 v189, s[36:37]
	s_mov_b32 m0, s55
	s_nop 0
	global_load_lds_dwordx4 v190, s[36:37]
	s_mov_b32 m0, s68
	s_waitcnt vmcnt(8)
	s_waitcnt lgkmcnt(0)
	s_barrier
	s_setprio 1
	s_waitcnt lgkmcnt(7)
	v_mfma_i32_16x16x64_i8 v[126:129], v[130:133], v[198:201], v[126:129]
	v_mfma_i32_16x16x64_i8 v[122:125], v[140:143], v[198:201], v[122:125]
	s_waitcnt lgkmcnt(5)
	v_mfma_i32_16x16x64_i8 v[118:121], v[130:133], v[206:209], v[118:121]
	v_mfma_i32_16x16x64_i8 v[106:109], v[140:143], v[206:209], v[106:109]
	s_waitcnt lgkmcnt(3)
	v_mfma_i32_16x16x64_i8 v[102:105], v[130:133], v[214:217], v[102:105]
	v_mfma_i32_16x16x64_i8 v[90:93], v[140:143], v[214:217], v[90:93]
	s_waitcnt lgkmcnt(1)
	v_mfma_i32_16x16x64_i8 v[86:89], v[130:133], v[222:225], v[86:89]
	v_mfma_i32_16x16x64_i8 v[74:77], v[140:143], v[222:225], v[74:77]
	v_mfma_i32_16x16x64_i8 v[126:129], v[134:137], v[202:205], v[126:129]
	v_mfma_i32_16x16x64_i8 v[122:125], v[144:147], v[202:205], v[122:125]
	v_mfma_i32_16x16x64_i8 v[118:121], v[134:137], v[210:213], v[118:121]
	v_mfma_i32_16x16x64_i8 v[106:109], v[144:147], v[210:213], v[106:109]
	v_mfma_i32_16x16x64_i8 v[102:105], v[134:137], v[218:221], v[102:105]
	v_mfma_i32_16x16x64_i8 v[90:93], v[144:147], v[218:221], v[90:93]
	s_waitcnt lgkmcnt(0)
	v_mfma_i32_16x16x64_i8 v[86:89], v[134:137], v[226:229], v[86:89]
	v_mfma_i32_16x16x64_i8 v[74:77], v[144:147], v[226:229], v[74:77]
	s_setprio 0
	s_setprio 1
	v_mfma_i32_16x16x64_i8 v[114:117], v[148:151], v[198:201], v[114:117]
	v_mfma_i32_16x16x64_i8 v[110:113], v[156:159], v[198:201], v[110:113]
	v_mfma_i32_16x16x64_i8 v[98:101], v[148:151], v[206:209], v[98:101]
	v_mfma_i32_16x16x64_i8 v[94:97], v[156:159], v[206:209], v[94:97]
	v_mfma_i32_16x16x64_i8 v[82:85], v[148:151], v[214:217], v[82:85]
	v_mfma_i32_16x16x64_i8 v[78:81], v[156:159], v[214:217], v[78:81]
	v_mfma_i32_16x16x64_i8 v[70:73], v[148:151], v[222:225], v[70:73]
	v_mfma_i32_16x16x64_i8 v[66:69], v[156:159], v[222:225], v[66:69]
	s_nop 0
	v_mfma_i32_16x16x64_i8 v[114:117], v[152:155], v[202:205], v[114:117]
	v_mfma_i32_16x16x64_i8 v[110:113], v[194:197], v[202:205], v[110:113]
	v_mfma_i32_16x16x64_i8 v[98:101], v[152:155], v[210:213], v[98:101]
	v_mfma_i32_16x16x64_i8 v[94:97], v[194:197], v[210:213], v[94:97]
	v_mfma_i32_16x16x64_i8 v[82:85], v[152:155], v[218:221], v[82:85]
	v_mfma_i32_16x16x64_i8 v[78:81], v[194:197], v[218:221], v[78:81]
	v_mfma_i32_16x16x64_i8 v[70:73], v[152:155], v[226:229], v[70:73]
	v_mfma_i32_16x16x64_i8 v[66:69], v[194:197], v[226:229], v[66:69]
	s_setprio 0
	s_barrier
; #define PG8_STAGEB(bufoff, gbase) glds2(voffB, (gbase), voffB, (gbase) + qstep, ldsb + (bufoff))
; #define PG8_STAGEA(bufoff, rowb, v, h, kb) do { if constexpr (GATHER) glds2((v)[h][0], Ab + (kb), (v)[h][1], Ab + (kb), ldsb + (bufoff)); \
;         else glds2(voffA, Ab + (rowb) + (h) * hstep + (kb), voffA, Ab + (rowb) + (h) * hstep + qstep + (kb), ldsb + (bufoff)); } while (0)
; #define PG8_LDA(dst, b, h) do { _Pragma("unroll") for (int m = 0; m < 4; ++m) _Pragma("unroll") for (int k = 0; k < 2; ++k) dst[m][k] = *(const PG8_LAS bf16x8*)(lds + PG8_SA(b, h) + aoff + m * 2048 + k * 1024); } while (0)
; #define PG8_LDB(dst, b, h) do { _Pragma("unroll") for (int n = 0; n < 2; ++n) _Pragma("unroll") for (int k = 0; k < 2; ++k) dst[n][k] = *(const PG8_LAS bf16x8*)(lds + PG8_SB(b, h) + boff + n * 2048 + k * 1024); } while (0)
; #define PG8_WAIT_V(n) asm volatile("s_waitcnt vmcnt(" #n ")" ::: "memory")
; #define PG8_WAIT_L(n) asm volatile("s_waitcnt lgkmcnt(" #n ")" ::: "memory")
; #define PG8_BAR __builtin_amdgcn_s_barrier()
; #define PG8_SCHED __builtin_amdgcn_sched_barrier(0)
; #define PG8_VOFF(dst, U) do { if constexpr (GATHER) { _Pragma("unroll") for (int h = 0; h < 2; ++h) _Pragma("unroll") for (int i = 0; i < 2; ++i) { \
;         const int row = g.rowidx[(U).pm * BM + h * HALF + i * 64 + R0]; dst[h][i] = (unsigned)row * (unsigned)RB + (unsigned)C0 * 2u; } } } while (0)
; template <class Epi, bool GATHER, int MODE, bool SPLIT = false>
; __device__ __forceinline__ void gemm_phase(PG8_LAS unsigned char* lds, const Gemm g, const Order& S, const Epi& E) {
;     ...
;         const bool has_next = S.next(ui + 1, nxt);
;         const char* nB = has_next ? (const char*)g.Bt + (size_t)nxt.e * g.bstride + (size_t)nxt.pn * tstep : cB;
;         const size_t nAr = has_next ? (size_t)nxt.pm * tstep : cAr;
;         if (has_next) { PG8_VOFF(nv, nxt); }
;     ...
;             PG8_LDA(At, 1, 1); PG8_STAGEB(PG8_SB(1, 0), b3); PG8_STAGEB(PG8_SB(1, 1), b3 + hstep); PG8_STAGEA(PG8_SA(1, 0), cAr, cv, 0, k3);
;             PG8_WAIT_V(8); PG8_WAIT_L(0); PG8_BAR; PG8_MMA(1, 0, At, B0); PG8_MMA(1, 1, At, B1); PG8_BAR; PG8_SCHED;
;         }
;         {
;             const size_t k1 = (size_t)(nt - 1) * kstep;
;             PG8_LDB(B0, 0, 0); PG8_LDB(B1, 0, 1); PG8_SCHED; PG8_LDA(At, 0, 0); PG8_STAGEA(PG8_SA(1, 1), cAr, cv, 1, k1);
	s_add_u32 s36, s66, 0x180
	s_addc_u32 s37, s67, 0
	s_add_u32 s68, s66, 0x20180
	s_addc_u32 s69, s67, 0
	ds_read_b128 v[198:201], v181 offset:49152
	ds_read_b128 v[202:205], v181 offset:50176
	ds_read_b128 v[206:209], v181 offset:51200
	ds_read_b128 v[210:213], v181 offset:52224
	ds_read_b128 v[214:217], v181 offset:53248
	ds_read_b128 v[218:221], v181 offset:54272
	ds_read_b128 v[222:225], v181 offset:55296
	ds_read_b128 v[226:229], v181 offset:56320
	s_mov_b32 s70, m0
	s_mov_b32 m0, s56
	s_nop 0
	global_load_lds_dwordx4 v168, s[36:37]
	s_mov_b32 m0, s57
	s_nop 0
	global_load_lds_dwordx4 v168, s[68:69]
	s_mov_b32 m0, s70
	s_add_u32 s36, s66, 0x40180
	s_addc_u32 s37, s67, 0
	s_add_u32 s66, s66, 0x60180
	s_addc_u32 s67, s67, 0
	s_mov_b32 s68, m0
	s_mov_b32 m0, s60
	s_nop 0
	global_load_lds_dwordx4 v168, s[36:37]
	s_mov_b32 m0, s61
	s_nop 0
	global_load_lds_dwordx4 v168, s[66:67]
	s_mov_b32 m0, s68
	s_add_u32 s36, s27, 0x180
	s_addc_u32 s37, s29, 0
	s_mov_b32 s27, m0
	s_mov_b32 m0, s58
	s_nop 0
	global_load_lds_dwordx4 v191, s[36:37]
	s_mov_b32 m0, s59
	s_nop 0
	global_load_lds_dwordx4 v192, s[36:37]
	s_mov_b32 m0, s27
	s_waitcnt vmcnt(8)
	s_waitcnt lgkmcnt(0)
	s_barrier
	s_setprio 1
	s_waitcnt lgkmcnt(7)
	v_mfma_i32_16x16x64_i8 v[62:65], v[130:133], v[198:201], v[62:65]
	v_mfma_i32_16x16x64_i8 v[58:61], v[140:143], v[198:201], v[58:61]
	s_waitcnt lgkmcnt(5)
	v_mfma_i32_16x16x64_i8 v[46:49], v[130:133], v[206:209], v[46:49]
	v_mfma_i32_16x16x64_i8 v[42:45], v[140:143], v[206:209], v[42:45]
	s_waitcnt lgkmcnt(3)
	v_mfma_i32_16x16x64_i8 v[38:41], v[130:133], v[214:217], v[38:41]
	v_mfma_i32_16x16x64_i8 v[34:37], v[140:143], v[214:217], v[34:37]
	s_waitcnt lgkmcnt(1)
	v_mfma_i32_16x16x64_i8 v[22:25], v[130:133], v[222:225], v[22:25]
	v_mfma_i32_16x16x64_i8 v[18:21], v[140:143], v[222:225], v[18:21]
	v_mfma_i32_16x16x64_i8 v[62:65], v[134:137], v[202:205], v[62:65]
	v_mfma_i32_16x16x64_i8 v[58:61], v[144:147], v[202:205], v[58:61]
	v_mfma_i32_16x16x64_i8 v[46:49], v[134:137], v[210:213], v[46:49]
	v_mfma_i32_16x16x64_i8 v[42:45], v[144:147], v[210:213], v[42:45]
	v_mfma_i32_16x16x64_i8 v[38:41], v[134:137], v[218:221], v[38:41]
	v_mfma_i32_16x16x64_i8 v[34:37], v[144:147], v[218:221], v[34:37]
	s_waitcnt lgkmcnt(0)
	v_mfma_i32_16x16x64_i8 v[22:25], v[134:137], v[226:229], v[22:25]
	v_mfma_i32_16x16x64_i8 v[18:21], v[144:147], v[226:229], v[18:21]
	s_setprio 0
	s_setprio 1
	v_mfma_i32_16x16x64_i8 v[54:57], v[148:151], v[198:201], v[54:57]
	v_mfma_i32_16x16x64_i8 v[50:53], v[156:159], v[198:201], v[50:53]
	v_mfma_i32_16x16x64_i8 v[30:33], v[148:151], v[206:209], v[30:33]
	v_mfma_i32_16x16x64_i8 v[26:29], v[156:159], v[206:209], v[26:29]
	v_mfma_i32_16x16x64_i8 v[14:17], v[148:151], v[214:217], v[14:17]
	v_mfma_i32_16x16x64_i8 v[10:13], v[156:159], v[214:217], v[10:13]
	v_mfma_i32_16x16x64_i8 v[6:9], v[148:151], v[222:225], v[6:9]
	v_mfma_i32_16x16x64_i8 v[2:5], v[156:159], v[222:225], v[2:5]
	s_nop 0
	v_mfma_i32_16x16x64_i8 v[54:57], v[152:155], v[202:205], v[54:57]
	v_mfma_i32_16x16x64_i8 v[50:53], v[194:197], v[202:205], v[50:53]
	v_mfma_i32_16x16x64_i8 v[30:33], v[152:155], v[210:213], v[30:33]
	v_mfma_i32_16x16x64_i8 v[26:29], v[194:197], v[210:213], v[26:29]
	v_mfma_i32_16x16x64_i8 v[14:17], v[152:155], v[218:221], v[14:17]
	v_mfma_i32_16x16x64_i8 v[10:13], v[194:197], v[218:221], v[10:13]
	v_mfma_i32_16x16x64_i8 v[6:9], v[152:155], v[226:229], v[6:9]
	v_mfma_i32_16x16x64_i8 v[2:5], v[194:197], v[226:229], v[2:5]
	s_setprio 0
	s_barrier
	s_add_i32 s11, s11, 2
	s_add_u32 s30, s30, 0x100
	s_addc_u32 s31, s31, 0
	s_cmp_lt_u32 s11, 12
	s_cbranch_scc1 .LBB0_802
	v_readfirstlane_b32 s28, v230
	s_and_b64 s[98:99], s[4:5], exec
	s_cbranch_scc0 .Lp8_nonext
	v_lshl_add_u32 v184, v231, 11, v167
	v_lshl_add_u32 v185, v232, 11, v167
	v_lshl_add_u32 v186, v233, 11, v167
	v_lshl_add_u32 v187, v234, 11, v167

; #define PG8_STAGEB(bufoff, gbase) glds2(voffB, (gbase), voffB, (gbase) + qstep, ldsb + (bufoff))
; #define PG8_BAR __builtin_amdgcn_s_barrier()
; template <class Epi, bool GATHER, int MODE, bool SPLIT = false>
; __device__ __forceinline__ void gemm_phase(PG8_LAS unsigned char* lds, const Gemm g, const Order& S, const Epi& E) {
;     ...
;     const int tid = tid_, wid = __builtin_amdgcn_readfirstlane(tid >> 6), lane = tid & 63, wr = wid >> 2, wc = wid & 3, fr = lane & 15, fq = lane >> 4;
;     const int RB = g.rowbytes, nt = RB / 128;
;     int R0, C0; stage_rc(tid * 16, R0, C0);
;     const int Rb0 = Epi::PERM ? ((R0 & ~31) + perm32(R0 & 31)) : R0;
;     const unsigned voffB = (unsigned)(Rb0 * RB + C0 * 2), voffA = (unsigned)(R0 * RB + C0 * 2);
;     const size_t kstep = (size_t)(BK * 2);
;     const size_t qstep = (size_t)64 * RB;
;     const size_t hstep = (size_t)HALF * RB;
;     const size_t tstep = 2 * hstep;
;     const unsigned ldsb = (unsigned)(size_t)lds + (unsigned)wid * 1024u;
;     const int aoff = lds_byte(wr * 64 + fr, fq * 8), boff = lds_byte(wc * 32 + fr, fq * 8);
;     ...
;     Unit cur, nxt; int ui = 0;
;     if (!S.next(0, cur)) return;
;     f32x4 acc[2][2][4][2];
; #pragma unroll
;     for (int a = 0; a < 2; ++a)
; #pragma unroll
;         for (int b = 0; b < 2; ++b)
; #pragma unroll
;             for (int m = 0; m < 4; ++m)
; #pragma unroll
;                 for (int n = 0; n < 2; ++n) acc[a][b][m][n] = (f32x4){0.f, 0.f, 0.f, 0.f};
;     bf16x8 At[4][2], B0[2][2], B1[2][2];
;     unsigned cv[2][2] = {{0u, 0u}, {0u, 0u}}, nv[2][2] = {{0u, 0u}, {0u, 0u}};
;     PG8_VOFF(cv, cur);
;     const char* const Ab = (const char*)g.A;
;     size_t cAr = (size_t)cur.pm * tstep;
;     const char* cB = (const char*)g.Bt + (size_t)cur.e * g.bstride + (size_t)cur.pn * tstep;
;     PG8_STAGEB(PG8_SB(0, 0), cB); PG8_STAGEB(PG8_SB(0, 1), cB + hstep); PG8_STAGEA(PG8_SA(0, 0), cAr, cv, 0, 0); PG8_STAGEA(PG8_SA(0, 1), cAr, cv, 1, 0);
;     if (wr == 1) PG8_BAR;
; __global__ void __launch_bounds__(NWAVES * 64, 2) fwd_kernel(Args args) {
;     ...
;     if (IN(9)) {
;         const int* TILEE = (const int*)(ws + WS_TILEE);
;         const int ntiles = __builtin_amdgcn_readfirstlane(TILEE[512]);
;         pg8::Gemm g{ws + WS_ACT, ws + WS_WD, DFF, (size_t)D * DFF, nullptr};
;         pg8::Order S; S.init(ntiles, D / 256, F.G, (int)blockIdx.x, TILEE, WGM_DN);
.LBB0_863:
	s_cmp_lt_i32 s78, 10
	s_cselect_b64 s[0:1], -1, 0
	s_cmp_gt_i32 s79, 9
	s_cselect_b64 s[2:3], -1, 0
	s_and_b64 s[0:1], s[0:1], s[2:3]
	s_andn2_b64 vcc, exec, s[0:1]
	s_cbranch_vccnz .LBB0_936
	v_mov_b32_e32 v1, 0xc00000
	global_load_dword v1, v1, s[76:77] offset:2048
	s_waitcnt vmcnt(20)
	v_mov_b32_e32 v2, v0
	s_waitcnt vmcnt(0)
	v_readfirstlane_b32 s11, v1
	s_lshl_b32 s2, s11, 3
	s_cmp_ge_i32 s92, s2
	v_readfirstlane_b32 s3, v2
	s_cbranch_scc1 .LBB0_882
	s_add_u32 s13, s76, 0xc00000
	s_addc_u32 s30, s77, 0
	s_add_u32 s31, s76, 2.0
	s_addc_u32 s34, s77, 0
	s_add_u32 s35, s76, 0x38000000
	s_addc_u32 s36, s77, 0
	s_ashr_i32 s10, s3, 6
	s_lshl_b32 s0, s10, 10
	s_ashr_i32 s38, s92, 31
	s_add_i32 s37, s0, 0
	s_lshr_b32 s0, s38, 29
	s_add_i32 s0, s92, s0
	s_ashr_i32 s1, s0, 3
	s_and_b32 s0, s0, -8
	s_ashr_i32 s12, s3, 8
	s_sub_i32 s0, s92, s0
	s_add_i32 s39, s11, 1
	s_cmp_lt_i32 s0, 0
	s_cselect_b32 s4, s39, s11
	s_mul_i32 s0, s4, s0
	s_add_i32 s0, s0, s1
	s_ashr_i32 s1, s0, 31
	s_lshr_b32 s1, s1, 27
	s_add_i32 s1, s0, s1
	s_ashr_i32 s4, s1, 5
	s_lshl_b32 s4, s4, 2
	s_sub_i32 s5, s11, s4
	s_min_i32 s5, s5, 4
	s_abs_i32 s6, s5
	v_cvt_f32_u32_e32 v1, s6
	s_sub_i32 s8, 0, s6
	s_andn2_b32 s1, s1, 31
	s_sub_i32 s0, s0, s1
	v_rcp_iflag_f32_e32 v1, v1
	s_abs_i32 s7, s0
	s_xor_b32 s1, s0, s5
	s_ashr_i32 s1, s1, 31
	v_mul_f32_e32 v1, 0x4f7ffffe, v1
	v_cvt_u32_f32_e32 v1, v1
	v_bfe_i32 v5, v2, 27, 1
	v_lshlrev_b32_e32 v3, 4, v2
	v_lshrrev_b32_e32 v5, 22, v5
	v_readfirstlane_b32 s9, v1
	s_mul_i32 s8, s8, s9
	s_mul_hi_u32 s8, s9, s8
	s_add_i32 s9, s9, s8
	s_mul_hi_u32 s8, s7, s9
	s_mul_i32 s9, s8, s6
	s_sub_i32 s7, s7, s9
	s_add_i32 s9, s8, 1
	s_sub_i32 s14, s7, s6
	s_cmp_ge_u32 s7, s6
	s_cselect_b32 s8, s9, s8
	s_cselect_b32 s7, s14, s7
	s_add_i32 s9, s8, 1
	s_cmp_ge_u32 s7, s6
	s_cselect_b32 s6, s9, s8
	s_xor_b32 s6, s6, s1
	s_sub_i32 s20, s6, s1
	s_mul_i32 s1, s20, s5
	s_sub_i32 s0, s0, s1
	s_add_i32 s0, s4, s0
	s_ashr_i32 s1, s0, 31
	s_lshl_b64 s[4:5], s[0:1], 2
	s_add_u32 s4, s13, s4
	s_addc_u32 s5, s30, s5
	v_mov_b32_e32 v1, 0
	global_load_dword v164, v1, s[4:5]
	v_add_u32_e32 v5, v3, v5
	v_and_b32_e32 v5, 0xfffffc00, v5
	v_sub_u32_e32 v3, v3, v5
	v_ashrrev_i32_e32 v4, 31, v2
	v_lshrrev_b32_e32 v7, 4, v3
	v_lshrrev_b32_e32 v4, 26, v4
	v_bitop3_b32 v3, v7, v3, 32 bitop3:0x6c
	v_add_u32_e32 v4, v2, v4
	v_ashrrev_i32_e32 v7, 31, v3
	v_ashrrev_i32_e32 v4, 6, v4
	v_lshrrev_b32_e32 v7, 26, v7
	v_lshlrev_b32_e32 v5, 3, v4
	v_add_u32_e32 v7, v3, v7
	v_and_b32_e32 v5, -16, v5
	v_ashrrev_i32_e32 v8, 6, v7
	v_and_b32_e32 v7, 0xc0, v7
	s_mov_b32 s4, 0x1fffe0
	v_add_u32_e32 v5, v8, v5
	v_sub_u32_e32 v3, v3, v7
	v_and_b32_e32 v7, 3, v8
	v_and_or_b32 v7, v5, s4, v7
	s_lshl_b64 s[22:23], s[0:1], 19
	v_mov_b32_e32 v6, 1
	v_lshlrev_b32_e32 v4, 5, v4
	v_ashrrev_i16_sdwa v3, v6, sext(v3) dst_sel:DWORD dst_unused:UNUSED_PAD src0_sel:DWORD src1_sel:BYTE_0
	v_lshlrev_b32_e32 v6, 1, v5
	v_lshrrev_b32_e32 v8, 2, v5
	v_and_b32_e32 v4, 32, v4
	v_bfe_i32 v3, v3, 0, 16
	v_and_b32_e32 v6, 24, v6
	v_and_b32_e32 v8, 4, v8
	v_or3_b32 v6, v7, v8, v6
	v_add_lshl_u32 v3, v4, v3, 1
	v_lshl_add_u32 v166, v6, 11, v3
	v_lshl_add_u32 v167, v5, 11, v3
	s_mov_b32 s40, 0
	s_waitcnt vmcnt(0)
	v_readfirstlane_b32 s4, v164
	s_ashr_i32 s5, s4, 31
	s_lshl_b64 s[4:5], s[4:5], 22
	s_add_u32 s1, s35, s4
	s_addc_u32 s6, s36, s5
	s_ashr_i32 s21, s20, 31
	s_lshl_b64 s[4:5], s[20:21], 19
	s_add_u32 s24, s1, s4
	s_addc_u32 s25, s6, s5
	s_add_u32 s4, s24, 0x20000
	s_addc_u32 s5, s25, 0
	s_add_i32 s21, s37, 0x10000
	s_add_i32 s41, s37, 0x12000
	s_mov_b32 s1, m0
	s_mov_b32 m0, s21
	s_nop 0
	global_load_lds_dwordx4 v166, s[24:25]
	s_mov_b32 m0, s41
	s_nop 0
	global_load_lds_dwordx4 v166, s[4:5]
	s_mov_b32 m0, s1
	s_add_u32 s4, s24, 0x40000
	s_addc_u32 s5, s25, 0
	s_add_u32 s6, s24, 0x60000
	s_addc_u32 s7, s25, 0
	s_add_i32 s42, s37, 0x14000
	s_add_i32 s43, s37, 0x16000
	s_add_u32 s8, s31, s22
	s_addc_u32 s9, s34, s23
	s_mov_b32 s1, m0
	s_mov_b32 m0, s42
	s_nop 0
	global_load_lds_dwordx4 v166, s[4:5]
	s_mov_b32 m0, s43
	s_nop 0
	global_load_lds_dwordx4 v166, s[6:7]
	s_mov_b32 m0, s1
	s_add_u32 s4, s8, 0x20000
	s_addc_u32 s5, s9, 0
	s_add_i32 s44, s37, 0x2000
	s_add_u32 s6, s8, 0x40000
	s_addc_u32 s7, s9, 0
	s_mov_b32 s1, m0
	s_mov_b32 m0, s37
	s_nop 0
	global_load_lds_dwordx4 v167, s[8:9]
	s_mov_b32 m0, s44
	s_nop 0
	global_load_lds_dwordx4 v167, s[4:5]
	s_mov_b32 m0, s1
	s_add_u32 s14, s8, 0x60000
	s_addc_u32 s15, s9, 0
	s_add_i32 s45, s37, 0x4000
	s_add_i32 s46, s37, 0x6000
	s_mov_b32 s1, m0
	s_mov_b32 m0, s45
	s_nop 0
	global_load_lds_dwordx4 v167, s[6:7]
	s_mov_b32 m0, s46
	s_nop 0
	global_load_lds_dwordx4 v167, s[14:15]
	s_mov_b32 m0, s1
	s_cmp_eq_u32 s12, 1
	s_cselect_b64 s[4:5], -1, 0
	s_cmp_lg_u32 s12, 1
	s_cbranch_scc1 .LBB0_867
	s_nop 0

; #define PG8_STAGEB(bufoff, gbase) glds2(voffB, (gbase), voffB, (gbase) + qstep, ldsb + (bufoff))
; #define PG8_STAGEA(bufoff, rowb, v, h, kb) do { if constexpr (GATHER) glds2((v)[h][0], Ab + (kb), (v)[h][1], Ab + (kb), ldsb + (bufoff)); \
;         else glds2(voffA, Ab + (rowb) + (h) * hstep + (kb), voffA, Ab + (rowb) + (h) * hstep + qstep + (kb), ldsb + (bufoff)); } while (0)
; #define PG8_LDA(dst, b, h) do { _Pragma("unroll") for (int m = 0; m < 4; ++m) _Pragma("unroll") for (int k = 0; k < 2; ++k) dst[m][k] = *(const PG8_LAS bf16x8*)(lds + PG8_SA(b, h) + aoff + m * 2048 + k * 1024); } while (0)
; #define PG8_LDB(dst, b, h) do { _Pragma("unroll") for (int n = 0; n < 2; ++n) _Pragma("unroll") for (int k = 0; k < 2; ++k) dst[n][k] = *(const PG8_LAS bf16x8*)(lds + PG8_SB(b, h) + boff + n * 2048 + k * 1024); } while (0)
; #define PG8_WAIT_V(n) asm volatile("s_waitcnt vmcnt(" #n ")" ::: "memory")
; #define PG8_WAIT_L(n) asm volatile("s_waitcnt lgkmcnt(" #n ")" ::: "memory")
; #define PG8_BAR __builtin_amdgcn_s_barrier()
; #define PG8_SCHED __builtin_amdgcn_sched_barrier(0)
; template <class Epi, bool GATHER, int MODE, bool SPLIT = false>
; __device__ __forceinline__ void gemm_phase(PG8_LAS unsigned char* lds, const Gemm g, const Order& S, const Epi& E) {
;     ...
;             const size_t k1 = (size_t)(t + 1) * kstep, k2 = k1 + kstep, k3 = k2 + kstep;
;             const char* b2 = cB + k2; const char* b3 = cB + k3;
;             PG8_LDB(B0, 0, 0); PG8_LDB(B1, 0, 1); PG8_SCHED; PG8_LDA(At, 0, 0); PG8_STAGEA(PG8_SA(1, 1), cAr, cv, 1, k1);
;             PG8_WAIT_V(8); PG8_WAIT_L(0); PG8_BAR; PG8_MMA(0, 0, At, B0); PG8_MMA(0, 1, At, B1); PG8_BAR; PG8_SCHED;
;             PG8_LDA(At, 0, 1); PG8_STAGEB(PG8_SB(0, 0), b2); PG8_STAGEB(PG8_SB(0, 1), b2 + hstep); PG8_STAGEA(PG8_SA(0, 0), cAr, cv, 0, k2);
;             PG8_WAIT_V(8); PG8_WAIT_L(0); PG8_BAR; PG8_MMA(1, 0, At, B0); PG8_MMA(1, 1, At, B1); PG8_BAR; PG8_SCHED;
;             PG8_LDB(B0, 1, 0); PG8_LDB(B1, 1, 1); PG8_SCHED; PG8_LDA(At, 1, 0); PG8_STAGEA(PG8_SA(0, 1), cAr, cv, 1, k2);
;             PG8_WAIT_V(8); PG8_WAIT_L(0); PG8_BAR; PG8_MMA(0, 0, At, B0); PG8_MMA(0, 1, At, B1); PG8_BAR; PG8_SCHED;
.LBB0_875:
	ds_read_b128 v[26:29], v172
	ds_read_b128 v[30:33], v172 offset:1024
	ds_read_b128 v[18:21], v172 offset:2048
	ds_read_b128 v[22:25], v172 offset:3072
	ds_read_b128 v[10:13], v173
	ds_read_b128 v[14:17], v173 offset:1024
	ds_read_b128 v[2:5], v173 offset:2048
	ds_read_b128 v[6:9], v173 offset:3072
	s_add_u32 s63, s24, s26
	s_addc_u32 s64, s25, s27
	s_add_u32 s28, s63, 0x100
	s_addc_u32 s29, s64, 0
	s_add_u32 s65, s15, s26
	ds_read_b128 v[180:183], v174
	ds_read_b128 v[184:187], v174 offset:1024
	ds_read_b128 v[188:191], v174 offset:2048
	ds_read_b128 v[192:195], v174 offset:3072
	ds_read_b128 v[196:199], v174 offset:4096
	ds_read_b128 v[200:203], v174 offset:5120
	ds_read_b128 v[204:207], v174 offset:6144
	ds_read_b128 v[208:211], v174 offset:7168
	s_addc_u32 s66, s19, s27
	s_add_u32 s70, s65, 0x80
	s_addc_u32 s71, s66, 0
	s_add_u32 s67, s58, s26
	s_addc_u32 s68, s59, s27
	s_add_u32 s80, s67, 0x80
	s_addc_u32 s81, s68, 0
	s_mov_b32 s69, m0
	s_mov_b32 m0, s53
	s_nop 0
	global_load_lds_dwordx4 v167, s[70:71]
	s_mov_b32 m0, s54
	s_nop 0
	global_load_lds_dwordx4 v167, s[80:81]
	s_mov_b32 m0, s69
	s_waitcnt vmcnt(8)
	s_waitcnt lgkmcnt(0)
	s_cmp_eq_i32 s62, -2
	s_cselect_b64 vcc, s[8:9], 0
	s_cbranch_vccnz .Lfb9
	s_barrier
.Lfb9:
	s_setprio 1
	s_waitcnt lgkmcnt(6)
	v_mfma_f32_16x16x128_f8f6f4 v[158:161], v[26:33], v[180:187], v[158:161]
	v_mfma_f32_16x16x128_f8f6f4 v[154:157], v[18:25], v[180:187], v[154:157]
	s_waitcnt lgkmcnt(4)
	v_mfma_f32_16x16x128_f8f6f4 v[150:153], v[26:33], v[188:195], v[150:153]
	v_mfma_f32_16x16x128_f8f6f4 v[146:149], v[18:25], v[188:195], v[146:149]
	s_waitcnt lgkmcnt(2)
	v_mfma_f32_16x16x128_f8f6f4 v[142:145], v[26:33], v[196:203], v[142:145]
	v_mfma_f32_16x16x128_f8f6f4 v[138:141], v[18:25], v[196:203], v[138:141]
	s_waitcnt lgkmcnt(0)
	v_mfma_f32_16x16x128_f8f6f4 v[134:137], v[26:33], v[204:211], v[134:137]
	v_mfma_f32_16x16x128_f8f6f4 v[130:133], v[18:25], v[204:211], v[130:133]
	s_setprio 0
	s_setprio 1
	v_mfma_f32_16x16x128_f8f6f4 v[126:129], v[10:17], v[180:187], v[126:129]
	v_mfma_f32_16x16x128_f8f6f4 v[122:125], v[2:9], v[180:187], v[122:125]
	v_mfma_f32_16x16x128_f8f6f4 v[118:121], v[10:17], v[188:195], v[118:121]
	v_mfma_f32_16x16x128_f8f6f4 v[114:117], v[2:9], v[188:195], v[114:117]
	v_mfma_f32_16x16x128_f8f6f4 v[110:113], v[10:17], v[196:203], v[110:113]
	v_mfma_f32_16x16x128_f8f6f4 v[106:109], v[2:9], v[196:203], v[106:109]
	v_mfma_f32_16x16x128_f8f6f4 v[102:105], v[10:17], v[204:211], v[102:105]
	v_mfma_f32_16x16x128_f8f6f4 v[98:101], v[2:9], v[204:211], v[98:101]
	s_setprio 0
	s_barrier
	s_add_u32 s70, s63, 0x20100
	s_addc_u32 s71, s64, 0
	ds_read_b128 v[180:183], v174 offset:16384
	ds_read_b128 v[184:187], v174 offset:17408
	ds_read_b128 v[188:191], v174 offset:18432
	ds_read_b128 v[192:195], v174 offset:19456
	ds_read_b128 v[196:199], v174 offset:20480
	ds_read_b128 v[200:203], v174 offset:21504
	ds_read_b128 v[204:207], v174 offset:22528
	ds_read_b128 v[208:211], v174 offset:23552
	s_mov_b32 s69, m0
	s_mov_b32 m0, s21
	s_nop 0
	global_load_lds_dwordx4 v166, s[28:29]
	s_mov_b32 m0, s41
	s_nop 0
	global_load_lds_dwordx4 v166, s[70:71]
	s_mov_b32 m0, s69
	s_add_u32 s28, s63, 0x40100
	s_addc_u32 s29, s64, 0
	s_add_u32 s70, s63, 0x60100
	s_addc_u32 s71, s64, 0
	s_mov_b32 s69, m0
	s_mov_b32 m0, s42
	s_nop 0
	global_load_lds_dwordx4 v166, s[28:29]
	s_mov_b32 m0, s43
	s_nop 0
	global_load_lds_dwordx4 v166, s[70:71]
	s_mov_b32 m0, s69
	s_add_u32 s28, s1, s26
	s_addc_u32 s29, s57, s27
	s_add_u32 s80, s28, 0x100
	s_addc_u32 s81, s29, 0
	s_add_u32 s69, s60, s26
	s_addc_u32 s70, s61, s27
	s_add_u32 s82, s69, 0x100
	s_addc_u32 s83, s70, 0
	s_mov_b32 s71, m0
	s_mov_b32 m0, s37
	s_nop 0
	global_load_lds_dwordx4 v167, s[80:81]
	s_mov_b32 m0, s44
	s_nop 0
	global_load_lds_dwordx4 v167, s[82:83]
	s_mov_b32 m0, s71
	s_waitcnt vmcnt(8)
	s_waitcnt lgkmcnt(0)
	s_barrier
	s_setprio 1
	s_waitcnt lgkmcnt(6)
	v_mfma_f32_16x16x128_f8f6f4 v[94:97], v[26:33], v[180:187], v[94:97]
	v_mfma_f32_16x16x128_f8f6f4 v[90:93], v[18:25], v[180:187], v[90:93]
	s_waitcnt lgkmcnt(4)
	v_mfma_f32_16x16x128_f8f6f4 v[86:89], v[26:33], v[188:195], v[86:89]
	v_mfma_f32_16x16x128_f8f6f4 v[82:85], v[18:25], v[188:195], v[82:85]
	s_waitcnt lgkmcnt(2)
	v_mfma_f32_16x16x128_f8f6f4 v[78:81], v[26:33], v[196:203], v[78:81]
	v_mfma_f32_16x16x128_f8f6f4 v[74:77], v[18:25], v[196:203], v[74:77]
	s_waitcnt lgkmcnt(0)
	v_mfma_f32_16x16x128_f8f6f4 v[70:73], v[26:33], v[204:211], v[70:73]
	v_mfma_f32_16x16x128_f8f6f4 v[66:69], v[18:25], v[204:211], v[66:69]
	s_setprio 0
	s_setprio 1
	v_mfma_f32_16x16x128_f8f6f4 v[62:65], v[10:17], v[180:187], v[62:65]
	v_mfma_f32_16x16x128_f8f6f4 v[58:61], v[2:9], v[180:187], v[58:61]
	v_mfma_f32_16x16x128_f8f6f4 v[54:57], v[10:17], v[188:195], v[54:57]
	v_mfma_f32_16x16x128_f8f6f4 v[50:53], v[2:9], v[188:195], v[50:53]
	v_mfma_f32_16x16x128_f8f6f4 v[46:49], v[10:17], v[196:203], v[46:49]
	v_mfma_f32_16x16x128_f8f6f4 v[42:45], v[2:9], v[196:203], v[42:45]
	v_mfma_f32_16x16x128_f8f6f4 v[38:41], v[10:17], v[204:211], v[38:41]
	v_mfma_f32_16x16x128_f8f6f4 v[34:37], v[2:9], v[204:211], v[34:37]
	s_setprio 0
	s_barrier
	ds_read_b128 v[18:21], v175
	ds_read_b128 v[22:25], v175 offset:1024
	ds_read_b128 v[26:29], v175 offset:2048
	ds_read_b128 v[30:33], v175 offset:3072
	ds_read_b128 v[10:13], v176
	ds_read_b128 v[14:17], v176 offset:1024
	ds_read_b128 v[2:5], v176 offset:2048
	ds_read_b128 v[6:9], v176 offset:3072
	ds_read_b128 v[180:183], v174 offset:32768
	ds_read_b128 v[184:187], v174 offset:33792
	ds_read_b128 v[188:191], v174 offset:34816
	ds_read_b128 v[192:195], v174 offset:35840
	ds_read_b128 v[196:199], v174 offset:36864
	ds_read_b128 v[200:203], v174 offset:37888
	ds_read_b128 v[204:207], v174 offset:38912
	ds_read_b128 v[208:211], v174 offset:39936
	s_add_u32 s80, s65, 0x100
	s_addc_u32 s81, s66, 0
	s_add_u32 s66, s67, 0x100
	s_addc_u32 s67, s68, 0
	s_mov_b32 s65, m0
	s_mov_b32 m0, s45
	s_nop 0
	global_load_lds_dwordx4 v167, s[80:81]
	s_mov_b32 m0, s46
	s_nop 0
	global_load_lds_dwordx4 v167, s[66:67]
	s_mov_b32 m0, s65
	s_waitcnt vmcnt(8)
	s_waitcnt lgkmcnt(0)
	s_barrier
; #define PG8_STAGEB(bufoff, gbase) glds2(voffB, (gbase), voffB, (gbase) + qstep, ldsb + (bufoff))
; #define PG8_STAGEA(bufoff, rowb, v, h, kb) do { if constexpr (GATHER) glds2((v)[h][0], Ab + (kb), (v)[h][1], Ab + (kb), ldsb + (bufoff)); \
;         else glds2(voffA, Ab + (rowb) + (h) * hstep + (kb), voffA, Ab + (rowb) + (h) * hstep + qstep + (kb), ldsb + (bufoff)); } while (0)
; #define PG8_LDA(dst, b, h) do { _Pragma("unroll") for (int m = 0; m < 4; ++m) _Pragma("unroll") for (int k = 0; k < 2; ++k) dst[m][k] = *(const PG8_LAS bf16x8*)(lds + PG8_SA(b, h) + aoff + m * 2048 + k * 1024); } while (0)
; #define PG8_LDB(dst, b, h) do { _Pragma("unroll") for (int n = 0; n < 2; ++n) _Pragma("unroll") for (int k = 0; k < 2; ++k) dst[n][k] = *(const PG8_LAS bf16x8*)(lds + PG8_SB(b, h) + boff + n * 2048 + k * 1024); } while (0)
; #define PG8_WAIT_V(n) asm volatile("s_waitcnt vmcnt(" #n ")" ::: "memory")
; #define PG8_WAIT_L(n) asm volatile("s_waitcnt lgkmcnt(" #n ")" ::: "memory")
; #define PG8_BAR __builtin_amdgcn_s_barrier()
; #define PG8_SCHED __builtin_amdgcn_sched_barrier(0)
; template <class Epi, bool GATHER, int MODE, bool SPLIT = false>
; __device__ __forceinline__ void gemm_phase(PG8_LAS unsigned char* lds, const Gemm g, const Order& S, const Epi& E) {
;     ...
;             PG8_LDA(At, 1, 1); PG8_STAGEB(PG8_SB(1, 0), b3); PG8_STAGEB(PG8_SB(1, 1), b3 + hstep); PG8_STAGEA(PG8_SA(1, 0), cAr, cv, 0, k3);
;             PG8_WAIT_V(8); PG8_WAIT_L(0); PG8_BAR; PG8_MMA(1, 0, At, B0); PG8_MMA(1, 1, At, B1); PG8_BAR; PG8_SCHED;
;         }
;         {
;             const size_t k1 = (size_t)(nt - 1) * kstep;
;             PG8_LDB(B0, 0, 0); PG8_LDB(B1, 0, 1); PG8_SCHED; PG8_LDA(At, 0, 0); PG8_STAGEA(PG8_SA(1, 1), cAr, cv, 1, k1);
	s_setprio 1
	s_waitcnt lgkmcnt(6)
	v_mfma_f32_16x16x128_f8f6f4 v[158:161], v[18:25], v[180:187], v[158:161]
	v_mfma_f32_16x16x128_f8f6f4 v[154:157], v[26:33], v[180:187], v[154:157]
	s_waitcnt lgkmcnt(4)
	v_mfma_f32_16x16x128_f8f6f4 v[150:153], v[18:25], v[188:195], v[150:153]
	v_mfma_f32_16x16x128_f8f6f4 v[146:149], v[26:33], v[188:195], v[146:149]
	s_waitcnt lgkmcnt(2)
	v_mfma_f32_16x16x128_f8f6f4 v[142:145], v[18:25], v[196:203], v[142:145]
	v_mfma_f32_16x16x128_f8f6f4 v[138:141], v[26:33], v[196:203], v[138:141]
	s_waitcnt lgkmcnt(0)
	v_mfma_f32_16x16x128_f8f6f4 v[134:137], v[18:25], v[204:211], v[134:137]
	v_mfma_f32_16x16x128_f8f6f4 v[130:133], v[26:33], v[204:211], v[130:133]
	s_setprio 0
	s_setprio 1
	v_mfma_f32_16x16x128_f8f6f4 v[126:129], v[10:17], v[180:187], v[126:129]
	v_mfma_f32_16x16x128_f8f6f4 v[122:125], v[2:9], v[180:187], v[122:125]
	v_mfma_f32_16x16x128_f8f6f4 v[118:121], v[10:17], v[188:195], v[118:121]
	v_mfma_f32_16x16x128_f8f6f4 v[114:117], v[2:9], v[188:195], v[114:117]
	v_mfma_f32_16x16x128_f8f6f4 v[110:113], v[10:17], v[196:203], v[110:113]
	v_mfma_f32_16x16x128_f8f6f4 v[106:109], v[2:9], v[196:203], v[106:109]
	v_mfma_f32_16x16x128_f8f6f4 v[102:105], v[10:17], v[204:211], v[102:105]
	v_mfma_f32_16x16x128_f8f6f4 v[98:101], v[2:9], v[204:211], v[98:101]
	s_setprio 0
	s_barrier
	s_add_u32 s66, s63, 0x180
	s_addc_u32 s67, s64, 0
	s_add_u32 s80, s63, 0x20180
	s_addc_u32 s81, s64, 0
	ds_read_b128 v[180:183], v174 offset:49152
	ds_read_b128 v[184:187], v174 offset:50176
	ds_read_b128 v[188:191], v174 offset:51200
	ds_read_b128 v[192:195], v174 offset:52224
	ds_read_b128 v[196:199], v174 offset:53248
	ds_read_b128 v[200:203], v174 offset:54272
	ds_read_b128 v[204:207], v174 offset:55296
	ds_read_b128 v[208:211], v174 offset:56320
	s_mov_b32 s65, m0
	s_mov_b32 m0, s47
	s_nop 0
	global_load_lds_dwordx4 v166, s[66:67]
	s_mov_b32 m0, s48
	s_nop 0
	global_load_lds_dwordx4 v166, s[80:81]
	s_mov_b32 m0, s65
	s_add_u32 s66, s63, 0x40180
	s_addc_u32 s67, s64, 0
	s_add_u32 s80, s63, 0x60180
	s_addc_u32 s81, s64, 0
	s_add_u32 s28, s28, 0x180
	s_addc_u32 s29, s29, 0
	s_mov_b32 s63, m0
	s_mov_b32 m0, s51
	s_nop 0
	global_load_lds_dwordx4 v166, s[66:67]
	s_mov_b32 m0, s52
	s_nop 0
	global_load_lds_dwordx4 v166, s[80:81]
	s_mov_b32 m0, s63
	s_add_u32 s64, s69, 0x180
	s_addc_u32 s65, s70, 0
	s_mov_b32 s63, m0
	s_mov_b32 m0, s49
	s_nop 0
	global_load_lds_dwordx4 v167, s[28:29]
	s_mov_b32 m0, s50
	s_nop 0
	global_load_lds_dwordx4 v167, s[64:65]
	s_mov_b32 m0, s63
	s_waitcnt vmcnt(8)
	s_waitcnt lgkmcnt(0)
	s_barrier
	s_setprio 1
	s_waitcnt lgkmcnt(6)
	v_mfma_f32_16x16x128_f8f6f4 v[94:97], v[18:25], v[180:187], v[94:97]
	v_mfma_f32_16x16x128_f8f6f4 v[90:93], v[26:33], v[180:187], v[90:93]
	s_waitcnt lgkmcnt(4)
	v_mfma_f32_16x16x128_f8f6f4 v[86:89], v[18:25], v[188:195], v[86:89]
	v_mfma_f32_16x16x128_f8f6f4 v[82:85], v[26:33], v[188:195], v[82:85]
	s_waitcnt lgkmcnt(2)
	v_mfma_f32_16x16x128_f8f6f4 v[78:81], v[18:25], v[196:203], v[78:81]
	v_mfma_f32_16x16x128_f8f6f4 v[74:77], v[26:33], v[196:203], v[74:77]
	s_waitcnt lgkmcnt(0)
	v_mfma_f32_16x16x128_f8f6f4 v[70:73], v[18:25], v[204:211], v[70:73]
	v_mfma_f32_16x16x128_f8f6f4 v[66:69], v[26:33], v[204:211], v[66:69]
	s_setprio 0
	s_setprio 1
	v_mfma_f32_16x16x128_f8f6f4 v[62:65], v[10:17], v[180:187], v[62:65]
	v_mfma_f32_16x16x128_f8f6f4 v[58:61], v[2:9], v[180:187], v[58:61]
	v_mfma_f32_16x16x128_f8f6f4 v[54:57], v[10:17], v[188:195], v[54:57]
	v_mfma_f32_16x16x128_f8f6f4 v[50:53], v[2:9], v[188:195], v[50:53]
	v_mfma_f32_16x16x128_f8f6f4 v[46:49], v[10:17], v[196:203], v[46:49]
	v_mfma_f32_16x16x128_f8f6f4 v[42:45], v[2:9], v[196:203], v[42:45]
	v_mfma_f32_16x16x128_f8f6f4 v[38:41], v[10:17], v[204:211], v[38:41]
	v_mfma_f32_16x16x128_f8f6f4 v[34:37], v[2:9], v[204:211], v[34:37]
	s_setprio 0
	s_barrier
	s_add_i32 s62, s62, 2
	s_add_u32 s26, s26, 0x100
	s_addc_u32 s27, s27, 0
	s_cmp_lt_u32 s62, 12
	s_cbranch_scc1 .LBB0_875
	v_readfirstlane_b32 s18, v230
	ds_read_b128 v[26:29], v172
	ds_read_b128 v[30:33], v172 offset:1024
	ds_read_b128 v[18:21], v172 offset:2048
	ds_read_b128 v[22:25], v172 offset:3072
	ds_read_b128 v[10:13], v173
	ds_read_b128 v[14:17], v173 offset:1024
	ds_read_b128 v[2:5], v173 offset:2048
	ds_read_b128 v[6:9], v173 offset:3072
	s_ashr_i32 s19, s18, 31
	s_lshl_b64 s[26:27], s[18:19], 22
	s_add_u32 s19, s35, s26
	s_addc_u32 s28, s36, s27
	s_ashr_i32 s15, s14, 31
	s_lshl_b64 s[26:27], s[14:15], 19
	s_add_u32 s26, s19, s26
	s_addc_u32 s27, s28, s27
	s_lshl_b64 s[28:29], s[16:17], 19
	s_and_b64 s[58:59], exec, s[2:3]
	s_cselect_b32 s25, s27, s25
	s_cselect_b32 s24, s26, s24
	s_cselect_b32 s15, s29, s23
	s_cselect_b32 s17, s28, s22
	ds_read_b128 v[180:183], v174
	ds_read_b128 v[184:187], v174 offset:1024
	ds_read_b128 v[188:191], v174 offset:2048
	ds_read_b128 v[192:195], v174 offset:3072
	ds_read_b128 v[196:199], v174 offset:4096
	ds_read_b128 v[200:203], v174 offset:5120
	ds_read_b128 v[204:207], v174 offset:6144
	ds_read_b128 v[208:211], v174 offset:7168
	s_add_u32 s22, s1, 0x40780
	s_addc_u32 s23, s57, 0
	s_add_u32 s58, s1, 0x60780
	s_addc_u32 s59, s57, 0
	s_mov_b32 s1, m0
	s_mov_b32 m0, s53
	s_nop 0
	global_load_lds_dwordx4 v167, s[22:23]
	s_mov_b32 m0, s54
	s_nop 0
	global_load_lds_dwordx4 v167, s[58:59]
	s_mov_b32 m0, s1
	s_waitcnt vmcnt(8)
	s_waitcnt lgkmcnt(0)
	s_barrier
; #define PG8_STAGEB(bufoff, gbase) glds2(voffB, (gbase), voffB, (gbase) + qstep, ldsb + (bufoff))
; #define PG8_STAGEA(bufoff, rowb, v, h, kb) do { if constexpr (GATHER) glds2((v)[h][0], Ab + (kb), (v)[h][1], Ab + (kb), ldsb + (bufoff)); \
;         else glds2(voffA, Ab + (rowb) + (h) * hstep + (kb), voffA, Ab + (rowb) + (h) * hstep + qstep + (kb), ldsb + (bufoff)); } while (0)
; #define PG8_LDA(dst, b, h) do { _Pragma("unroll") for (int m = 0; m < 4; ++m) _Pragma("unroll") for (int k = 0; k < 2; ++k) dst[m][k] = *(const PG8_LAS bf16x8*)(lds + PG8_SA(b, h) + aoff + m * 2048 + k * 1024); } while (0)
; #define PG8_LDB(dst, b, h) do { _Pragma("unroll") for (int n = 0; n < 2; ++n) _Pragma("unroll") for (int k = 0; k < 2; ++k) dst[n][k] = *(const PG8_LAS bf16x8*)(lds + PG8_SB(b, h) + boff + n * 2048 + k * 1024); } while (0)
; #define PG8_WAIT_V(n) asm volatile("s_waitcnt vmcnt(" #n ")" ::: "memory")
; #define PG8_WAIT_L(n) asm volatile("s_waitcnt lgkmcnt(" #n ")" ::: "memory")
; #define PG8_BAR __builtin_amdgcn_s_barrier()
; #define PG8_SCHED __builtin_amdgcn_sched_barrier(0)
; template <class Epi, bool GATHER, int MODE, bool SPLIT = false>
; __device__ __forceinline__ void gemm_phase(PG8_LAS unsigned char* lds, const Gemm g, const Order& S, const Epi& E) {
;     ...
;             PG8_LDB(B0, 0, 0); PG8_LDB(B1, 0, 1); PG8_SCHED; PG8_LDA(At, 0, 0); PG8_STAGEA(PG8_SA(1, 1), cAr, cv, 1, k1);
;             PG8_WAIT_V(8); PG8_WAIT_L(0); PG8_BAR; PG8_MMA(0, 0, At, B0); PG8_MMA(0, 1, At, B1); PG8_BAR; PG8_SCHED;
;             PG8_LDA(At, 0, 1); PG8_STAGEB(PG8_SB(0, 0), nB); PG8_STAGEB(PG8_SB(0, 1), nB + hstep); PG8_STAGEA(PG8_SA(0, 0), nAr, nv, 0, 0);
;             PG8_WAIT_V(8); PG8_WAIT_L(0); PG8_BAR; PG8_MMA(1, 0, At, B0); PG8_MMA(1, 1, At, B1); PG8_BAR; PG8_SCHED;
;             PG8_LDB(B0, 1, 0); PG8_LDB(B1, 1, 1); PG8_SCHED; PG8_LDA(At, 1, 0); PG8_STAGEA(PG8_SA(0, 1), nAr, nv, 1, 0);
;             PG8_WAIT_V(8); PG8_WAIT_L(0); PG8_BAR; PG8_MMA(0, 0, At, B0); PG8_MMA(0, 1, At, B1); PG8_BAR; PG8_SCHED;
	s_setprio 1
	s_waitcnt lgkmcnt(6)
	v_mfma_f32_16x16x128_f8f6f4 v[158:161], v[26:33], v[180:187], v[158:161]
	v_mfma_f32_16x16x128_f8f6f4 v[154:157], v[18:25], v[180:187], v[154:157]
	s_waitcnt lgkmcnt(4)
	v_mfma_f32_16x16x128_f8f6f4 v[150:153], v[26:33], v[188:195], v[150:153]
	v_mfma_f32_16x16x128_f8f6f4 v[146:149], v[18:25], v[188:195], v[146:149]
	s_waitcnt lgkmcnt(2)
	v_mfma_f32_16x16x128_f8f6f4 v[142:145], v[26:33], v[196:203], v[142:145]
	v_mfma_f32_16x16x128_f8f6f4 v[138:141], v[18:25], v[196:203], v[138:141]
	s_waitcnt lgkmcnt(0)
	v_mfma_f32_16x16x128_f8f6f4 v[134:137], v[26:33], v[204:211], v[134:137]
	v_mfma_f32_16x16x128_f8f6f4 v[130:133], v[18:25], v[204:211], v[130:133]
	s_setprio 0
	s_setprio 1
	v_mfma_f32_16x16x128_f8f6f4 v[126:129], v[10:17], v[180:187], v[126:129]
	v_mfma_f32_16x16x128_f8f6f4 v[122:125], v[2:9], v[180:187], v[122:125]
	v_mfma_f32_16x16x128_f8f6f4 v[118:121], v[10:17], v[188:195], v[118:121]
	v_mfma_f32_16x16x128_f8f6f4 v[114:117], v[2:9], v[188:195], v[114:117]
	v_mfma_f32_16x16x128_f8f6f4 v[110:113], v[10:17], v[196:203], v[110:113]
	v_mfma_f32_16x16x128_f8f6f4 v[106:109], v[2:9], v[196:203], v[106:109]
	v_mfma_f32_16x16x128_f8f6f4 v[102:105], v[10:17], v[204:211], v[102:105]
	v_mfma_f32_16x16x128_f8f6f4 v[98:101], v[2:9], v[204:211], v[98:101]
	s_setprio 0
	s_barrier
	s_add_u32 s22, s24, 0x20000
	s_addc_u32 s23, s25, 0
	ds_read_b128 v[180:183], v174 offset:16384
	ds_read_b128 v[184:187], v174 offset:17408
	ds_read_b128 v[188:191], v174 offset:18432
	ds_read_b128 v[192:195], v174 offset:19456
	ds_read_b128 v[196:199], v174 offset:20480
	ds_read_b128 v[200:203], v174 offset:21504
	ds_read_b128 v[204:207], v174 offset:22528
	ds_read_b128 v[208:211], v174 offset:23552
	s_mov_b32 s1, m0
	s_mov_b32 m0, s21
	s_nop 0
	global_load_lds_dwordx4 v166, s[24:25]
	s_mov_b32 m0, s41
	s_nop 0
	global_load_lds_dwordx4 v166, s[22:23]
	s_mov_b32 m0, s1
	s_add_u32 s22, s24, 0x40000
	s_addc_u32 s23, s25, 0
	s_add_u32 s58, s24, 0x60000
	s_addc_u32 s59, s25, 0
	s_mov_b32 s1, m0
	s_mov_b32 m0, s42
	s_nop 0
	global_load_lds_dwordx4 v166, s[22:23]
	s_mov_b32 m0, s43
	s_nop 0
	global_load_lds_dwordx4 v166, s[58:59]
	s_mov_b32 m0, s1
	s_add_u32 s22, s31, s17
	s_addc_u32 s23, s34, s15
	s_add_u32 s58, s22, 0x20000
	s_addc_u32 s59, s23, 0
	s_mov_b32 s1, m0
	s_mov_b32 m0, s37
	s_nop 0
	global_load_lds_dwordx4 v167, s[22:23]
	s_mov_b32 m0, s44
	s_nop 0
	global_load_lds_dwordx4 v167, s[58:59]
	s_mov_b32 m0, s1
	s_waitcnt vmcnt(8)
	s_waitcnt lgkmcnt(0)
	s_barrier
	s_setprio 1
	s_waitcnt lgkmcnt(6)
	v_mfma_f32_16x16x128_f8f6f4 v[94:97], v[26:33], v[180:187], v[94:97]
	v_mfma_f32_16x16x128_f8f6f4 v[90:93], v[18:25], v[180:187], v[90:93]
	s_waitcnt lgkmcnt(4)
	v_mfma_f32_16x16x128_f8f6f4 v[86:89], v[26:33], v[188:195], v[86:89]
	v_mfma_f32_16x16x128_f8f6f4 v[82:85], v[18:25], v[188:195], v[82:85]
	s_waitcnt lgkmcnt(2)
	v_mfma_f32_16x16x128_f8f6f4 v[78:81], v[26:33], v[196:203], v[78:81]
	v_mfma_f32_16x16x128_f8f6f4 v[74:77], v[18:25], v[196:203], v[74:77]
	s_waitcnt lgkmcnt(0)
	v_mfma_f32_16x16x128_f8f6f4 v[70:73], v[26:33], v[204:211], v[70:73]
	v_mfma_f32_16x16x128_f8f6f4 v[66:69], v[18:25], v[204:211], v[66:69]
	s_setprio 0
	s_setprio 1
	v_mfma_f32_16x16x128_f8f6f4 v[62:65], v[10:17], v[180:187], v[62:65]
	v_mfma_f32_16x16x128_f8f6f4 v[58:61], v[2:9], v[180:187], v[58:61]
	v_mfma_f32_16x16x128_f8f6f4 v[54:57], v[10:17], v[188:195], v[54:57]
	v_mfma_f32_16x16x128_f8f6f4 v[50:53], v[2:9], v[188:195], v[50:53]
	v_mfma_f32_16x16x128_f8f6f4 v[46:49], v[10:17], v[196:203], v[46:49]
	v_mfma_f32_16x16x128_f8f6f4 v[42:45], v[2:9], v[196:203], v[42:45]
	v_mfma_f32_16x16x128_f8f6f4 v[38:41], v[10:17], v[204:211], v[38:41]
	v_mfma_f32_16x16x128_f8f6f4 v[34:37], v[2:9], v[204:211], v[34:37]
	s_setprio 0
	s_barrier
	ds_read_b128 v[26:29], v175
	ds_read_b128 v[30:33], v175 offset:1024
	ds_read_b128 v[18:21], v175 offset:2048
	ds_read_b128 v[22:25], v175 offset:3072
	ds_read_b128 v[10:13], v176
	ds_read_b128 v[14:17], v176 offset:1024
	ds_read_b128 v[2:5], v176 offset:2048
	ds_read_b128 v[6:9], v176 offset:3072
	ds_read_b128 v[180:183], v174 offset:32768
	ds_read_b128 v[184:187], v174 offset:33792
	ds_read_b128 v[188:191], v174 offset:34816
	ds_read_b128 v[192:195], v174 offset:35840
	ds_read_b128 v[196:199], v174 offset:36864
	ds_read_b128 v[200:203], v174 offset:37888
	ds_read_b128 v[204:207], v174 offset:38912
	ds_read_b128 v[208:211], v174 offset:39936
	s_add_u32 s58, s22, 0x40000
	s_addc_u32 s59, s23, 0
	s_add_u32 s60, s22, 0x60000
	s_addc_u32 s61, s23, 0
	s_mov_b32 s1, m0
	s_mov_b32 m0, s45
	s_nop 0
	global_load_lds_dwordx4 v167, s[58:59]
	s_mov_b32 m0, s46
	s_nop 0
	global_load_lds_dwordx4 v167, s[60:61]
	s_mov_b32 m0, s1
	s_waitcnt vmcnt(8)
	s_waitcnt lgkmcnt(0)
	s_barrier
; #define PG8_STAGEB(bufoff, gbase) glds2(voffB, (gbase), voffB, (gbase) + qstep, ldsb + (bufoff))
; #define PG8_STAGEA(bufoff, rowb, v, h, kb) do { if constexpr (GATHER) glds2((v)[h][0], Ab + (kb), (v)[h][1], Ab + (kb), ldsb + (bufoff)); \
;         else glds2(voffA, Ab + (rowb) + (h) * hstep + (kb), voffA, Ab + (rowb) + (h) * hstep + qstep + (kb), ldsb + (bufoff)); } while (0)
; #define PG8_LDA(dst, b, h) do { _Pragma("unroll") for (int m = 0; m < 4; ++m) _Pragma("unroll") for (int k = 0; k < 2; ++k) dst[m][k] = *(const PG8_LAS bf16x8*)(lds + PG8_SA(b, h) + aoff + m * 2048 + k * 1024); } while (0)
; #define PG8_WAIT_V(n) asm volatile("s_waitcnt vmcnt(" #n ")" ::: "memory")
; #define PG8_WAIT_L(n) asm volatile("s_waitcnt lgkmcnt(" #n ")" ::: "memory")
; #define PG8_BAR __builtin_amdgcn_s_barrier()
; #define PG8_SCHED __builtin_amdgcn_sched_barrier(0)
; template <class Epi, bool GATHER, int MODE, bool SPLIT = false>
; __device__ __forceinline__ void gemm_phase(PG8_LAS unsigned char* lds, const Gemm g, const Order& S, const Epi& E) {
;     ...
;             PG8_WAIT_V(8); PG8_WAIT_L(0); PG8_BAR; PG8_MMA(0, 0, At, B0); PG8_MMA(0, 1, At, B1); PG8_BAR; PG8_SCHED;
;             PG8_LDA(At, 1, 1); PG8_STAGEB(PG8_SB(1, 0), nB + kstep); PG8_STAGEB(PG8_SB(1, 1), nB + hstep + kstep); PG8_STAGEA(PG8_SA(1, 0), nAr, nv, 0, kstep);
;             PG8_WAIT_V(8); PG8_WAIT_L(0); PG8_BAR; PG8_MMA(1, 0, At, B0); PG8_MMA(1, 1, At, B1); PG8_BAR; PG8_SCHED;
;         }
;         if (wr == 0) PG8_BAR;
	s_setprio 1
	s_waitcnt lgkmcnt(6)
	v_mfma_f32_16x16x128_f8f6f4 v[158:161], v[26:33], v[180:187], v[158:161]
	v_mfma_f32_16x16x128_f8f6f4 v[154:157], v[18:25], v[180:187], v[154:157]
	s_waitcnt lgkmcnt(4)
	v_mfma_f32_16x16x128_f8f6f4 v[150:153], v[26:33], v[188:195], v[150:153]
	v_mfma_f32_16x16x128_f8f6f4 v[146:149], v[18:25], v[188:195], v[146:149]
	s_waitcnt lgkmcnt(2)
	v_mfma_f32_16x16x128_f8f6f4 v[142:145], v[26:33], v[196:203], v[142:145]
	v_mfma_f32_16x16x128_f8f6f4 v[138:141], v[18:25], v[196:203], v[138:141]
	s_waitcnt lgkmcnt(0)
	v_mfma_f32_16x16x128_f8f6f4 v[134:137], v[26:33], v[204:211], v[134:137]
	v_mfma_f32_16x16x128_f8f6f4 v[130:133], v[18:25], v[204:211], v[130:133]
	s_setprio 0
	s_setprio 1
	v_mfma_f32_16x16x128_f8f6f4 v[126:129], v[10:17], v[180:187], v[126:129]
	v_mfma_f32_16x16x128_f8f6f4 v[122:125], v[2:9], v[180:187], v[122:125]
	v_mfma_f32_16x16x128_f8f6f4 v[118:121], v[10:17], v[188:195], v[118:121]
	v_mfma_f32_16x16x128_f8f6f4 v[114:117], v[2:9], v[188:195], v[114:117]
	v_mfma_f32_16x16x128_f8f6f4 v[110:113], v[10:17], v[196:203], v[110:113]
	v_mfma_f32_16x16x128_f8f6f4 v[106:109], v[2:9], v[196:203], v[106:109]
	v_mfma_f32_16x16x128_f8f6f4 v[102:105], v[10:17], v[204:211], v[102:105]
	v_mfma_f32_16x16x128_f8f6f4 v[98:101], v[2:9], v[204:211], v[98:101]
	s_setprio 0
	s_barrier
	s_add_u32 s58, s24, 0x80
	s_addc_u32 s59, s25, 0
	s_add_u32 s60, s24, 0x20080
	s_addc_u32 s61, s25, 0
	ds_read_b128 v[180:183], v174 offset:49152
	ds_read_b128 v[184:187], v174 offset:50176
	ds_read_b128 v[188:191], v174 offset:51200
	ds_read_b128 v[192:195], v174 offset:52224
	ds_read_b128 v[196:199], v174 offset:53248
	ds_read_b128 v[200:203], v174 offset:54272
	ds_read_b128 v[204:207], v174 offset:55296
	ds_read_b128 v[208:211], v174 offset:56320
	s_mov_b32 s1, m0
	s_mov_b32 m0, s47
	s_nop 0
	global_load_lds_dwordx4 v166, s[58:59]
	s_mov_b32 m0, s48
	s_nop 0
	global_load_lds_dwordx4 v166, s[60:61]
	s_mov_b32 m0, s1
	s_add_u32 s58, s24, 0x40080
	s_addc_u32 s59, s25, 0
	s_add_u32 s24, s24, 0x60080
	s_addc_u32 s25, s25, 0
	s_mov_b32 s1, m0
	s_mov_b32 m0, s51
	s_nop 0
	global_load_lds_dwordx4 v166, s[58:59]
	s_mov_b32 m0, s52
	s_nop 0
	global_load_lds_dwordx4 v166, s[24:25]
	s_mov_b32 m0, s1
	s_add_u32 s24, s22, 0x80
	s_addc_u32 s25, s23, 0
	s_add_u32 s22, s22, 0x20080
	s_addc_u32 s23, s23, 0
	s_mov_b32 s1, m0
	s_mov_b32 m0, s49
	s_nop 0
	global_load_lds_dwordx4 v167, s[24:25]
	s_mov_b32 m0, s50
	s_nop 0
	global_load_lds_dwordx4 v167, s[22:23]
	s_mov_b32 m0, s1
	s_waitcnt vmcnt(8)
	s_waitcnt lgkmcnt(0)
	s_barrier
	s_setprio 1
	s_waitcnt lgkmcnt(6)
	v_mfma_f32_16x16x128_f8f6f4 v[94:97], v[26:33], v[180:187], v[94:97]
	v_mfma_f32_16x16x128_f8f6f4 v[90:93], v[18:25], v[180:187], v[90:93]
	s_waitcnt lgkmcnt(4)
	v_mfma_f32_16x16x128_f8f6f4 v[86:89], v[26:33], v[188:195], v[86:89]
	v_mfma_f32_16x16x128_f8f6f4 v[82:85], v[18:25], v[188:195], v[82:85]
	s_waitcnt lgkmcnt(2)
	v_mfma_f32_16x16x128_f8f6f4 v[78:81], v[26:33], v[196:203], v[78:81]
	v_mfma_f32_16x16x128_f8f6f4 v[74:77], v[18:25], v[196:203], v[74:77]
	s_waitcnt lgkmcnt(0)
	v_mfma_f32_16x16x128_f8f6f4 v[70:73], v[26:33], v[204:211], v[70:73]
	v_mfma_f32_16x16x128_f8f6f4 v[66:69], v[18:25], v[204:211], v[66:69]
	s_setprio 0
	s_setprio 1
	v_mfma_f32_16x16x128_f8f6f4 v[62:65], v[10:17], v[180:187], v[62:65]
	v_mfma_f32_16x16x128_f8f6f4 v[58:61], v[2:9], v[180:187], v[58:61]
	v_mfma_f32_16x16x128_f8f6f4 v[54:57], v[10:17], v[188:195], v[54:57]
	v_mfma_f32_16x16x128_f8f6f4 v[50:53], v[2:9], v[188:195], v[50:53]
	v_mfma_f32_16x16x128_f8f6f4 v[46:49], v[10:17], v[196:203], v[46:49]
	v_mfma_f32_16x16x128_f8f6f4 v[42:45], v[2:9], v[196:203], v[42:45]
	v_mfma_f32_16x16x128_f8f6f4 v[38:41], v[10:17], v[204:211], v[38:41]
	v_mfma_f32_16x16x128_f8f6f4 v[34:37], v[2:9], v[204:211], v[34:37]
	s_setprio 0
	s_nop 0
	s_andn2_b64 vcc, exec, s[8:9]
	s_cbranch_vccnz .LBB0_878
	s_barrier
